# edge1: last six row gathers of a tile issued right after the MFMA that frees their registers instead of ~130 instructions later
# speedup vs baseline: 1.0042x; 1.0042x over previous
.Lprio_e1_done:
	s_mov_b32 s93, s94
	s_add_u32 s94, s94, 0x1000
	s_cmp_lt_u32 s94, 0x61a8
	s_cselect_b32 s95, s94, s93
	s_lshl_b32 s95, s95, 9
	s_add_u32 s56, s8, s95
	s_addc_u32 s57, s9, 0
	ds_bpermute_b32 v126, v125, v51
	v_sub_f32_e32 v39, v48, v67
	v_fmamk_f32 v32, v39, 0x4297576a, v65
	v_fmamk_f32 v33, v39, 0x4297576a, v76
	v_med3_f32 v35, v32, s22, v74
	v_med3_f32 v37, v33, s22, v74
	v_mul_f32_e64 v32, v35, -v35
	v_fmamk_f32 v34, v35, 0x4019be61, v75
	v_mul_f32_e64 v33, v37, -v37
	v_fmamk_f32 v35, v35, 0xc019be61, v75
	v_exp_f32_e32 v32, v32
	v_exp_f32_e32 v33, v33
	v_exp_f32_e32 v36, v35
	v_fmamk_f32 v35, v37, 0x4019be61, v75
	v_exp_f32_e32 v34, v34
	v_exp_f32_e32 v35, v35
	v_fmamk_f32 v37, v37, 0xc019be61, v75
	v_exp_f32_e32 v37, v37
	v_pk_mul_f32 v[32:33], v[48:49], v[32:33] op_sel:[1,0]
	ds_read_b128 v[28:31], v69
	ds_read_b128 v[24:27], v69 offset:1024
	ds_read_b128 v[20:23], v69 offset:2048
	ds_read_b128 v[16:19], v69 offset:3072
	ds_read_b128 v[0:3], v70
	ds_read_b128 v[4:7], v70 offset:32
	ds_read_b128 v[8:11], v70 offset:64
	ds_read_b128 v[12:15], v70 offset:96
	v_pk_mul_f32 v[44:45], v[34:35], v[32:33]
	v_pk_mul_f32 v[34:35], v[34:35], s[16:17] op_sel_hi:[1,0]
	v_mov_b32_e32 v99, v80
	v_fmamk_f32 v38, v39, 0x4297576a, v77
	v_fmamk_f32 v39, v39, 0x4297576a, v78
	v_pk_mul_f32 v[46:47], v[34:35], v[44:45]
	v_pk_mul_f32 v[34:35], v[34:35], s[16:17] op_sel_hi:[1,0]
	v_pk_mul_f32 v[80:81], v[36:37], v[32:33]
	v_pk_mul_f32 v[36:37], v[36:37], s[16:17] op_sel_hi:[1,0]
	v_med3_f32 v41, v38, s22, v74
	v_med3_f32 v43, v39, s22, v74
	v_pk_mul_f32 v[58:59], v[34:35], v[46:47]
	v_pk_mul_f32 v[34:35], v[34:35], s[16:17] op_sel_hi:[1,0]
	v_pk_mul_f32 v[82:83], v[36:37], v[80:81]
	v_pk_mul_f32 v[36:37], v[36:37], s[16:17] op_sel_hi:[1,0]
	v_mul_f32_e64 v38, v41, -v41
	v_fmamk_f32 v40, v41, 0x4019be61, v75
	v_mul_f32_e64 v39, v43, -v43
	v_fmamk_f32 v41, v41, 0xc019be61, v75
	v_pk_mul_f32 v[34:35], v[34:35], v[58:59]
	v_pk_mul_f32 v[36:37], v[36:37], v[82:83]
	v_exp_f32_e32 v38, v38
	v_exp_f32_e32 v39, v39
	v_exp_f32_e32 v42, v41
	v_fmamk_f32 v41, v43, 0x4019be61, v75
	v_cvt_pk_f16_f32 v56, v44, v46
	v_cvt_pk_f16_f32 v54, v36, v82
	v_cvt_pk_f16_f32 v57, v58, v34
	v_cvt_pk_f16_f32 v55, v80, v32
	v_exp_f32_e32 v40, v40
	v_exp_f32_e32 v41, v41
	s_waitcnt lgkmcnt(0)
	v_mfma_f32_32x32x16_f16 v[0:15], v[28:31], v[54:57], v[0:15]
	v_mul_f32_e64 v38, v49, v38
	v_mul_f32_e64 v39, v49, v39
	v_fmamk_f32 v43, v43, 0xc019be61, v75
	v_mul_f32_e64 v84, v40, v38
	v_mul_f32_e64 v85, v41, v39
	v_pk_mul_f32 v[40:41], v[40:41], s[16:17] op_sel_hi:[1,0]
	v_cvt_pk_f16_f32 v30, v45, v47
	v_pk_mul_f32 v[86:87], v[40:41], v[84:85]
	v_pk_mul_f32 v[28:29], v[40:41], s[16:17] op_sel_hi:[1,0]
	v_cvt_pk_f16_f32 v31, v59, v35
	v_pk_mul_f32 v[40:41], v[28:29], v[86:87]
	v_pk_mul_f32 v[28:29], v[28:29], s[16:17] op_sel_hi:[1,0]
	v_exp_f32_e32 v43, v43
	v_pk_mul_f32 v[88:89], v[28:29], v[40:41]
	v_cvt_pk_f16_f32 v28, v37, v83
	v_cvt_pk_f16_f32 v29, v81, v33
	v_pk_mul_f32 v[36:37], v[42:43], v[38:39]
	v_pk_mul_f32 v[42:43], v[42:43], s[16:17] op_sel_hi:[1,0]
	v_mfma_f32_32x32x16_f16 v[0:15], v[24:27], v[28:31], v[0:15]
	v_mul_f32_e64 v32, v42, v36
	v_mul_f32_e64 v33, v43, v37
	v_mul_f32_e64 v24, v42, s16
	v_mul_f32_e64 v25, v43, s16
	v_cvt_pk_f16_f32 v26, v84, v86
	v_pk_mul_f32 v[34:35], v[24:25], v[32:33]
	v_cvt_pk_f16_f32 v27, v40, v88
	v_cvt_pk_f16_f32 v24, v34, v32
	v_cvt_pk_f16_f32 v25, v36, v38
	v_cvt_pk_f16_f32 v84, v85, v87
	v_cvt_pk_f16_f32 v82, v35, v33
	v_mfma_f32_32x32x16_f16 v[0:15], v[20:23], v[24:27], v[0:15]
	ds_read_b128 v[20:23], v69 offset:4096
	v_cvt_pk_f16_f32 v85, v41, v89
	v_cvt_pk_f16_f32 v83, v37, v39
	ds_read_b128 v[32:35], v70 offset:128
	ds_read_b128 v[36:39], v70 offset:160
	ds_read_b128 v[40:43], v70 offset:192
	ds_read_b128 v[44:47], v70 offset:224
	s_nop 0
	v_add_u32_e32 v64, s12, v64
	v_perm_b32 v127, v126, v51, s64
	s_nop 0
	v_readlane_b32 s70, v127, 0
	v_readlane_b32 s71, v127, 1
	v_readlane_b32 s72, v127, 2
	v_readlane_b32 s73, v127, 3
	v_readlane_b32 s74, v127, 4
	v_readlane_b32 s75, v127, 5
	v_readlane_b32 s76, v127, 6
	v_readlane_b32 s77, v127, 7
	v_readlane_b32 s78, v127, 8
	v_readlane_b32 s79, v127, 9
	v_readlane_b32 s80, v127, 10
	v_readlane_b32 s81, v127, 11
	v_readlane_b32 s82, v127, 12
	v_readlane_b32 s83, v127, 13
	v_readlane_b32 s84, v127, 14
	v_readlane_b32 s85, v127, 15
	s_pack_ll_b32_b16 s48, s70, 0
	v_mfma_f32_32x32x16_f16 v[0:15], v[16:19], v[82:85], v[0:15]
	ds_read_b128 v[16:19], v69 offset:5120
	s_nop 0
	s_lshl_b32 s48, s48, 8
	s_and_b32 s48, s48, 0xffff00
	s_pack_ll_b32_b16 s47, s71, 0
	s_add_u32 s48, s4, s48
	s_addc_u32 s49, s5, 0
	s_waitcnt lgkmcnt(1)
	v_mfma_f32_32x32x16_f16 v[32:47], v[20:23], v[54:57], v[32:47]
	ds_read_b128 v[20:23], v69 offset:6144
	s_lshl_b32 s47, s47, 8
	s_and_b32 s47, s47, 0xffff00
	s_pack_ll_b32_b16 s46, s72, 0
	s_pack_ll_b32_b16 s45, s73, 0
	s_pack_ll_b32_b16 s44, s74, 0
	s_pack_ll_b32_b16 s43, s75, 0
	s_waitcnt lgkmcnt(1)
	v_mfma_f32_32x32x16_f16 v[32:47], v[16:19], v[28:31], v[32:47]
	s_nop 0
	s_nop 0
	s_mov_b64 vcc, 0
	s_nop 0
	s_nop 0
	s_pack_ll_b32_b16 s3, s76, 0
	s_pack_ll_b32_b16 s2, s77, 0
	s_waitcnt lgkmcnt(0)
	v_mfma_f32_32x32x16_f16 v[32:47], v[20:23], v[24:27], v[32:47]
	s_nop 0
	s_nop 0
	s_pack_ll_b32_b16 s36, s78, 0
	s_pack_ll_b32_b16 s35, s79, 0
	s_pack_ll_b32_b16 s34, s80, 0
	s_pack_ll_b32_b16 s33, s81, 0
	s_pack_ll_b32_b16 s31, s82, 0
	s_pack_ll_b32_b16 s30, s83, 0
	s_pack_ll_b32_b16 s29, s84, 0
	s_pack_ll_b32_b16 s28, s85, 0
	s_pack_hh_b32_b16 s27, s70, 0
	s_pack_hh_b32_b16 s26, s71, 0
	s_pack_hh_b32_b16 s25, s72, 0
	s_pack_hh_b32_b16 s24, s73, 0
	s_pack_hh_b32_b16 s23, s74, 0
	s_pack_hh_b32_b16 s42, s75, 0
	s_pack_hh_b32_b16 s41, s76, 0
	s_pack_hh_b32_b16 s40, s77, 0
	s_pack_hh_b32_b16 s39, s78, 0
	s_pack_hh_b32_b16 s38, s79, 0
	s_pack_hh_b32_b16 s37, s80, 0
	s_pack_hh_b32_b16 s21, s81, 0
	s_pack_hh_b32_b16 s20, s82, 0
	s_pack_hh_b32_b16 s19, s83, 0
	s_pack_hh_b32_b16 s18, s84, 0
	s_pack_hh_b32_b16 s10, s85, 0
	ds_read_b128 v[16:19], v69 offset:7168
	s_nop 0
	global_load_dwordx4 v[56:59], v124, s[56:57]
	global_load_dword v80, v124, s[56:57] offset:24
	global_load_dword v51, v124, s[56:57] offset:-8
	global_load_dword v112, v79, s[48:49]
	s_add_u32 s48, s4, s47
	s_addc_u32 s49, s5, 0
	s_lshl_b32 s46, s46, 8
	s_and_b32 s46, s46, 0xffff00
	s_add_u32 s46, s4, s46
	s_addc_u32 s47, s5, 0
	s_lshl_b32 s45, s45, 8
	s_and_b32 s45, s45, 0xffff00
	global_load_dword v110, v79, s[48:49]
	global_load_dword v108, v79, s[46:47]
	s_add_u32 s46, s4, s45
	s_addc_u32 s47, s5, 0
	s_lshl_b32 s44, s44, 8
	s_and_b32 s44, s44, 0xffff00
	s_add_u32 s44, s4, s44
	s_addc_u32 s45, s5, 0
	s_lshl_b32 s43, s43, 8
	s_and_b32 s43, s43, 0xffff00
	global_load_dword v106, v79, s[46:47]
	global_load_dword v104, v79, s[44:45]
	s_add_u32 s44, s4, s43
	s_addc_u32 s45, s5, 0
	s_lshl_b32 s3, s3, 8
	s_and_b32 s3, s3, 0xffff00
	global_load_dword v102, v79, s[44:45]
	s_add_u32 s44, s4, s3
	s_addc_u32 s45, s5, 0
	s_lshl_b32 s2, s2, 8
	s_and_b32 s2, s2, 0xffff00
	s_add_u32 s2, s4, s2
	global_load_dword v100, v79, s[44:45]
	s_addc_u32 s3, s5, 0
	global_load_dword v114, v79, s[2:3]
	s_lshl_b32 s2, s36, 8
	s_and_b32 s2, s2, 0xffff00
	s_add_u32 s2, s4, s2
	s_addc_u32 s3, s5, 0
	global_load_dword v113, v79, s[2:3]
	s_lshl_b32 s2, s35, 8
	s_and_b32 s2, s2, 0xffff00
	s_add_u32 s2, s4, s2
	s_addc_u32 s3, s5, 0
	global_load_dword v111, v79, s[2:3]
	s_lshl_b32 s2, s34, 8
	s_and_b32 s2, s2, 0xffff00
	s_add_u32 s2, s4, s2
	s_addc_u32 s3, s5, 0
	global_load_dword v109, v79, s[2:3]
	s_lshl_b32 s2, s33, 8
	s_and_b32 s2, s2, 0xffff00
	s_add_u32 s2, s4, s2
	s_addc_u32 s3, s5, 0
	global_load_dword v107, v79, s[2:3]
	s_lshl_b32 s2, s31, 8
	s_and_b32 s2, s2, 0xffff00
	s_add_u32 s2, s4, s2
	s_addc_u32 s3, s5, 0
	global_load_dword v105, v79, s[2:3]
	s_lshl_b32 s2, s30, 8
	s_and_b32 s2, s2, 0xffff00
	s_add_u32 s2, s4, s2
	s_addc_u32 s3, s5, 0
	global_load_dword v103, v79, s[2:3]
	s_lshl_b32 s2, s29, 8
	s_and_b32 s2, s2, 0xffff00
	s_add_u32 s2, s4, s2
	s_addc_u32 s3, s5, 0
	global_load_dword v101, v79, s[2:3]
	s_lshl_b32 s2, s28, 8
	s_and_b32 s2, s2, 0xffff00
	s_add_u32 s2, s4, s2
	s_addc_u32 s3, s5, 0
	global_load_dword v98, v79, s[2:3]
	s_lshl_b32 s2, s27, 8
	s_and_b32 s2, s2, 0xffff00
	s_add_u32 s2, s4, s2
	s_addc_u32 s3, s5, 0
	global_load_dword v97, v79, s[2:3]
	s_lshl_b32 s2, s26, 8
	s_and_b32 s2, s2, 0xffff00
	s_add_u32 s2, s4, s2
	s_addc_u32 s3, s5, 0
	global_load_dword v96, v79, s[2:3]
	s_lshl_b32 s2, s25, 8
	s_and_b32 s2, s2, 0xffff00
	s_add_u32 s2, s4, s2
	s_addc_u32 s3, s5, 0
	global_load_dword v94, v79, s[2:3]
	s_lshl_b32 s2, s24, 8
	s_and_b32 s2, s2, 0xffff00
	s_add_u32 s2, s4, s2
	s_addc_u32 s3, s5, 0
	global_load_dword v91, v79, s[2:3]
	s_lshl_b32 s2, s23, 8
	s_and_b32 s2, s2, 0xffff00
	s_add_u32 s2, s4, s2
	s_addc_u32 s3, s5, 0
	global_load_dword v93, v79, s[2:3]
	s_lshl_b32 s2, s42, 8
	s_and_b32 s2, s2, 0xffff00
	s_add_u32 s2, s4, s2
	s_addc_u32 s3, s5, 0
	global_load_dword v90, v79, s[2:3]
	s_lshl_b32 s2, s41, 8
	s_and_b32 s2, s2, 0xffff00
	s_add_u32 s2, s4, s2
	s_addc_u32 s3, s5, 0
	global_load_dword v88, v79, s[2:3]
	s_lshl_b32 s2, s40, 8
	s_and_b32 s2, s2, 0xffff00
	s_add_u32 s2, s4, s2
	s_addc_u32 s3, s5, 0
	global_load_dword v86, v79, s[2:3]
	s_lshl_b32 s2, s39, 8
	s_and_b32 s2, s2, 0xffff00
	s_nop 0
	s_nop 0
	s_add_u32 s2, s4, s2
	s_waitcnt lgkmcnt(0)
	v_mfma_f32_32x32x16_f16 v[32:47], v[16:19], v[82:85], v[32:47]
	v_exp_f32_e32 v0, v0
	v_exp_f32_e32 v1, v1
	s_addc_u32 s3, s5, 0
	global_load_dword v85, v79, s[2:3]
	s_lshl_b32 s2, s38, 8
	s_and_b32 s2, s2, 0xffff00
	s_nop 0
	s_nop 0
	s_add_u32 s2, s4, s2
	v_exp_f32_e32 v6, v6
	v_exp_f32_e32 v7, v7
	s_addc_u32 s3, s5, 0
	global_load_dword v83, v79, s[2:3]
	s_lshl_b32 s2, s37, 8
	s_and_b32 s2, s2, 0xffff00
	s_add_u32 s2, s4, s2
	s_addc_u32 s3, s5, 0
	global_load_dword v92, v79, s[2:3]
	s_lshl_b32 s2, s21, 8
	s_and_b32 s2, s2, 0xffff00
	s_add_u32 s2, s4, s2
	s_addc_u32 s3, s5, 0
	global_load_dword v89, v79, s[2:3]
	s_lshl_b32 s2, s20, 8
	s_and_b32 s2, s2, 0xffff00
	s_add_u32 s2, s4, s2
	s_addc_u32 s3, s5, 0
	s_lshl_b32 s19, s19, 8
	s_and_b32 s19, s19, 0xffff00
	s_add_u32 s20, s4, s19
	s_addc_u32 s21, s5, 0
	s_lshl_b32 s18, s18, 8
	s_and_b32 s18, s18, 0xffff00
	s_add_u32 s18, s4, s18
	s_addc_u32 s19, s5, 0
	s_lshl_b32 s10, s10, 8
	s_and_b32 s10, s10, 0xffff00
	s_add_u32 s24, s4, s10
	s_addc_u32 s25, s5, 0
	global_load_dword v87, v79, s[2:3]
	global_load_dword v84, v79, s[20:21]
	global_load_dword v82, v79, s[18:19]
	global_load_dword v81, v79, s[24:25]
	v_pk_add_f32 v[0:1], v[0:1], 1.0 op_sel_hi:[1,0]
	s_nop 0
	s_nop 0
	v_exp_f32_e32 v16, v4
	v_exp_f32_e32 v17, v5
	v_log_f32_e32 v4, v0
	v_log_f32_e32 v5, v1
	s_nop 0
	s_nop 0
	v_exp_f32_e32 v2, v2
	v_exp_f32_e32 v3, v3
	v_pk_add_f32 v[6:7], v[6:7], 1.0 op_sel_hi:[1,0]
	v_log_f32_e32 v6, v6
	v_log_f32_e32 v7, v7
	v_pk_add_f32 v[0:1], v[16:17], 1.0 op_sel_hi:[1,0]
	v_pk_add_f32 v[2:3], v[2:3], 1.0 op_sel_hi:[1,0]
	v_log_f32_e32 v0, v0
	v_log_f32_e32 v1, v1
	v_exp_f32_e32 v18, v8
	v_exp_f32_e32 v19, v9
	v_log_f32_e32 v8, v2
	v_log_f32_e32 v9, v3
	v_pk_mul_f32 v[2:3], v[48:49], v[6:7] op_sel:[1,0]
	s_nop 0
	s_nop 0
	v_pk_mul_f32 v[0:1], v[48:49], v[0:1] op_sel:[1,0]
	s_nop 0
	s_nop 0
	v_cvt_pk_f16_f32 v3, v2, v3
	v_cvt_pk_f16_f32 v2, v0, v1
	v_pk_mul_f32 v[0:1], v[48:49], v[8:9] op_sel:[1,0]
	v_pk_mul_f32 v[4:5], v[48:49], v[4:5] op_sel:[1,0]
	s_nop 0
	s_nop 0
	s_nop 0
	s_nop 0
	v_cvt_pk_f16_f32 v1, v0, v1
	v_cvt_pk_f16_f32 v0, v4, v5
	v_pk_add_f32 v[4:5], v[18:19], 1.0 op_sel_hi:[1,0]
	v_exp_f32_e32 v6, v10
	v_exp_f32_e32 v7, v11
	v_exp_f32_e32 v8, v12
	v_exp_f32_e32 v9, v13
	v_exp_f32_e32 v10, v14
	v_exp_f32_e32 v11, v15
	v_pk_add_f32 v[8:9], v[8:9], 1.0 op_sel_hi:[1,0]
	v_pk_add_f32 v[10:11], v[10:11], 1.0 op_sel_hi:[1,0]
	v_pk_add_f32 v[6:7], v[6:7], 1.0 op_sel_hi:[1,0]
	v_log_f32_e32 v8, v8
	v_log_f32_e32 v9, v9
	v_log_f32_e32 v10, v10
	v_log_f32_e32 v11, v11
	ds_read_b128 v[12:15], v71
	v_log_f32_e32 v6, v6
	v_log_f32_e32 v7, v7
	v_log_f32_e32 v4, v4
	v_log_f32_e32 v5, v5
	v_pk_mul_f32 v[8:9], v[48:49], v[8:9] op_sel:[1,0]
	v_pk_mul_f32 v[10:11], v[48:49], v[10:11] op_sel:[1,0]
	v_cvt_pk_f16_f32 v118, v8, v9
	v_cvt_pk_f16_f32 v119, v10, v11
	v_pk_mul_f32 v[10:11], v[48:49], v[6:7] op_sel:[1,0]
	ds_read_b128 v[6:9], v71 offset:1024
	s_waitcnt lgkmcnt(1)
	v_mfma_f32_32x32x16_f16 v[16:31], v[0:3], v[12:15], 0
	s_nop 0
	s_nop 0
	v_mul_f32_e64 v4, v49, v4
	v_mul_f32_e64 v5, v49, v5
	v_exp_f32_e32 v32, v32
	v_exp_f32_e32 v33, v33
	s_nop 0
	s_nop 0
	v_cvt_pk_f16_f32 v117, v10, v11
	v_cvt_pk_f16_f32 v116, v4, v5
	v_exp_f32_e32 v36, v36
	v_exp_f32_e32 v37, v37
	v_pk_add_f32 v[32:33], v[32:33], 1.0 op_sel_hi:[1,0]
	s_waitcnt lgkmcnt(0)
	v_mfma_f32_32x32x16_f16 v[16:31], v[116:119], v[6:9], v[16:31]
	v_log_f32_e32 v54, v32
	v_log_f32_e32 v55, v33
	v_pk_add_f32 v[32:33], v[36:37], 1.0 op_sel_hi:[1,0]
	s_nop 0
	s_nop 0
	ds_read_b128 v[4:7], v71 offset:4096
	ds_read_b128 v[120:123], v71 offset:5120
	v_exp_f32_e32 v36, v38
	v_exp_f32_e32 v37, v39
	s_nop 0
	s_nop 0
	s_waitcnt lgkmcnt(1)
	v_mfma_f32_32x32x16_f16 v[0:15], v[0:3], v[4:7], 0
	v_exp_f32_e32 v34, v34
	v_exp_f32_e32 v35, v35
	v_pk_add_f32 v[36:37], v[36:37], 1.0 op_sel_hi:[1,0]
	v_log_f32_e32 v32, v32
	v_log_f32_e32 v33, v33
	v_log_f32_e32 v36, v36
	v_log_f32_e32 v37, v37
	v_pk_add_f32 v[34:35], v[34:35], 1.0 op_sel_hi:[1,0]
	v_pk_mul_f32 v[32:33], v[48:49], v[32:33] op_sel:[1,0]
	v_log_f32_e32 v38, v34
	v_log_f32_e32 v39, v35
	v_pk_mul_f32 v[34:35], v[48:49], v[36:37] op_sel:[1,0]
	v_pk_mul_f32 v[36:37], v[48:49], v[54:55] op_sel:[1,0]
	v_cvt_pk_f16_f32 v35, v34, v35
	v_cvt_pk_f16_f32 v34, v32, v33
	v_pk_mul_f32 v[32:33], v[48:49], v[38:39] op_sel:[1,0]
	s_waitcnt lgkmcnt(0)
	v_mfma_f32_32x32x16_f16 v[0:15], v[116:119], v[120:123], v[0:15]
	v_cvt_pk_f16_f32 v33, v32, v33
	v_cvt_pk_f16_f32 v32, v36, v37
	ds_read_b128 v[36:39], v71 offset:2048
	ds_read_b128 v[116:119], v71 offset:3072
	s_nop 0
	s_nop 0
	v_exp_f32_e32 v55, v44
	v_exp_f32_e32 v115, v45
	s_waitcnt lgkmcnt(1)
	v_mfma_f32_32x32x16_f16 v[16:31], v[32:35], v[36:39], v[16:31]
	ds_read_b128 v[36:39], v71 offset:6144
	v_exp_f32_e32 v44, v40
	v_exp_f32_e32 v45, v41
	v_exp_f32_e32 v52, v42
	v_exp_f32_e32 v54, v43
	ds_read_b128 v[40:43], v71 offset:7168
	s_nop 0
	s_waitcnt lgkmcnt(1)
	v_mfma_f32_32x32x16_f16 v[0:15], v[32:35], v[36:39], v[0:15]
	v_add_f32_e64 v34, v44, 1.0
	v_add_f32_e64 v35, v45, 1.0
	s_nop 0
	s_nop 0
	s_nop 0
	v_log_f32_e32 v36, v34
	v_log_f32_e32 v37, v35
	v_exp_f32_e32 v34, v46
	v_exp_f32_e32 v35, v47
	s_nop 0
	s_nop 0
	v_add_f32_e64 v32, v55, 1.0
	v_add_f32_e64 v33, v115, 1.0
	v_pk_add_f32 v[34:35], v[34:35], 1.0 op_sel_hi:[1,0]
	v_log_f32_e32 v32, v32
	v_log_f32_e32 v33, v33
	v_log_f32_e32 v34, v34
	v_log_f32_e32 v35, v35
	v_add_f32_e64 v38, v52, 1.0
	v_add_f32_e64 v39, v54, 1.0
	v_pk_mul_f32 v[32:33], v[48:49], v[32:33] op_sel:[1,0]
	v_log_f32_e32 v38, v38
	v_log_f32_e32 v39, v39
	v_pk_mul_f32 v[34:35], v[48:49], v[34:35] op_sel:[1,0]
	v_pk_mul_f32 v[36:37], v[48:49], v[36:37] op_sel:[1,0]
	v_cvt_pk_f16_f32 v35, v34, v35
	v_cvt_pk_f16_f32 v34, v32, v33
	v_pk_mul_f32 v[32:33], v[48:49], v[38:39] op_sel:[1,0]
	v_mov_b32_e32 v54, v53
	v_cvt_pk_f16_f32 v33, v32, v33
	v_cvt_pk_f16_f32 v32, v36, v37
	v_cvt_f16_f32_e32 v36, v49
	v_mov_b32_e32 v55, v53
	v_mfma_f32_32x32x16_f16 v[16:31], v[32:35], v[116:119], v[16:31]
	v_cmp_ne_u32_sdwa s[20:21], v95, v50 src0_sel:DWORD src1_sel:WORD_1
	v_cmp_ne_u32_sdwa s[18:19], v99, v50 src0_sel:WORD_1 src1_sel:WORD_1
	s_bitcmp1_b32 s20, 0
	v_cmp_lt_i32_e64 s[2:3], s13, v64
	s_cselect_b64 s[20:21], -1, 0
	s_bitcmp0_b32 s18, 0
	s_waitcnt lgkmcnt(0)
	v_mfma_f32_32x32x16_f16 v[0:15], v[32:35], v[40:43], v[0:15]
	v_cndmask_b32_e64 v32, 0, v36, s[0:1]
	v_pack_b32_f16 v52, v32, 0
	ds_read_b128 v[32:35], v72
	ds_read_b128 v[36:39], v72 offset:1024
	s_waitcnt vmcnt(0)
	s_waitcnt vmcnt(0)
	s_waitcnt lgkmcnt(1)
	v_mfma_f32_32x32x16_f16 v[16:31], v[52:55], v[32:35], v[16:31]
	v_mov_b64_e32 v[32:33], 0
	s_nop 0
	s_waitcnt lgkmcnt(0)
	v_mfma_f32_32x32x16_f16 v[0:15], v[52:55], v[36:39], v[0:15]
	s_nop 11
	v_permlane32_swap_b32_e32 v16, v0
	v_permlane32_swap_b32_e32 v17, v1
	v_permlane32_swap_b32_e32 v18, v2
	v_permlane32_swap_b32_e32 v19, v3
	v_permlane32_swap_b32_e32 v20, v4
	v_permlane32_swap_b32_e32 v21, v5
	v_permlane32_swap_b32_e32 v22, v6
	v_permlane32_swap_b32_e32 v23, v7
	v_permlane32_swap_b32_e32 v24, v8
	v_permlane32_swap_b32_e32 v25, v9
	v_permlane32_swap_b32_e32 v26, v10
	v_permlane32_swap_b32_e32 v27, v11
	v_permlane32_swap_b32_e32 v28, v12
	v_permlane32_swap_b32_e32 v29, v13
	v_permlane32_swap_b32_e32 v30, v14
	v_permlane32_swap_b32_e32 v31, v15
	v_fma_mix_f32 v32, v16, v112, v32 op_sel:[0,1,0] op_sel_hi:[0,1,0]
	v_fma_mix_f32 v33, v16, v112, v33 op_sel_hi:[0,1,0]
	s_cbranch_scc1 .LBB4_13
	v_readlane_b32 s10, v50, 0
	s_bfe_u32 s19, s10, 0x80008
	v_lshl_or_b32 v16, s19, 7, v73
	ds_read_u16 v16, v16
	s_bfe_u32 s10, s10, 0x100010
	s_lshl_b32 s10, s10, 8
	s_add_u32 s58, s60, s10
	s_addc_u32 s59, s61, 0
	s_cmp_lg_u64 s[20:21], 0
	s_cselect_b32 s58, s58, s62
	s_cselect_b32 s59, s59, s63
	s_nop 0
	s_waitcnt lgkmcnt(0)
	v_fma_mix_f32 v16, v16, v33, v32 op_sel_hi:[1,0,0]
	s_nop 0
	s_mov_b64 s[20:21], -1
	v_mov_b64_e32 v[32:33], 0
	s_nop 0
	global_store_dword v79, v16, s[58:59] sc1
